# adds fp6 GEMM LDS chunk swizzle (conflict-free 8-byte fragment reads) on top of gate-gather batching
# speedup vs baseline: 1.0125x; 1.0067x over previous
.LBB0_680:
	s_andn2_b64 vcc, exec, s[38:39]
	s_cbranch_vccnz .LBB0_754
	s_ashr_i32 s1, s30, 31
	s_lshr_b32 s1, s1, 26
	s_add_i32 s1, s30, s1
	s_ashr_i32 s1, s1, 6
	s_mul_i32 s23, s1, 0x6000
	s_ashr_i32 s26, s65, 31
	s_mul_hi_i32 s17, s1, 0x6000
	s_mul_i32 s26, s23, s26
	s_mul_hi_u32 s27, s23, s65
	s_ashr_i32 s7, s29, 6
	s_add_i32 s26, s27, s26
	s_mul_i32 s27, s17, s65
	s_ashr_i32 s10, s29, 8
	s_lshl_b32 s11, s7, 10
	s_add_i32 s26, s26, s27
	s_mul_i32 s27, s23, s65
	s_add_u32 s38, s3, s27
	s_addc_u32 s39, s5, s26
	s_ashr_i32 s26, s64, 31
	s_mul_i32 s26, s23, s26
	s_mul_hi_u32 s27, s23, s64
	s_add_i32 s26, s27, s26
	s_mul_i32 s27, s17, s64
	s_add_i32 s26, s26, s27
	s_mul_i32 s27, s23, s64
	s_add_u32 s40, s8, s27
	s_addc_u32 s41, s12, s26
	s_add_i32 s26, s11, 0
	v_lshlrev_b32_e32 v0, 4, v2
	v_add_u32_e32 v210, 0x2000, v0
	v_add_u32_e32 v212, 0x4000, v0
	v_mul_u32_u24_e32 v218, 0x2aab, v2
	v_bfe_u32 v218, v218, 19, 1
	v_lshlrev_b32_e32 v218, 4, v218
	v_xor_b32_e32 v0, v0, v218
	v_add_u32_e32 v218, 0x200, v2
	v_mul_u32_u24_e32 v218, 0x2aab, v218
	v_bfe_u32 v218, v218, 19, 1
	v_lshlrev_b32_e32 v218, 4, v218
	v_xor_b32_e32 v210, v210, v218
	v_add_u32_e32 v218, 0x400, v2
	v_mul_u32_u24_e32 v218, 0x2aab, v218
	v_bfe_u32 v218, v218, 19, 1
	v_lshlrev_b32_e32 v218, 4, v218
	v_xor_b32_e32 v212, v212, v218
	s_add_i32 s11, s26, 0x6000
	s_mov_b32 m0, s26
	global_load_lds_dwordx4 v0, s[38:39]
	s_mov_b32 m0, s11
	global_load_lds_dwordx4 v0, s[40:41]
	s_add_i32 m0, s26, 0x2000
	s_nop 0
	global_load_lds_dwordx4 v210, s[38:39]
	s_add_i32 m0, s26, 0x8000
	s_nop 0
	global_load_lds_dwordx4 v210, s[40:41]
	s_add_i32 m0, s26, 0x4000
	s_nop 0
	global_load_lds_dwordx4 v212, s[38:39]
	s_add_i32 m0, s26, 0xa000
	s_add_u32 s36, s38, 0x6000
	global_load_lds_dwordx4 v212, s[40:41]
	s_addc_u32 s37, s39, 0
	s_add_i32 m0, s26, 0xc000
	s_add_u32 s44, s40, 0x6000
	s_addc_u32 s45, s41, 0
	s_add_i32 s11, s26, 0x12000
	global_load_lds_dwordx4 v0, s[36:37]
	s_mov_b32 m0, s11
	s_nop 0
	global_load_lds_dwordx4 v0, s[44:45]
	s_add_i32 m0, s26, 0xe000
	s_nop 0
	global_load_lds_dwordx4 v210, s[36:37]
	s_add_i32 m0, s26, 0x14000
	s_nop 0
	global_load_lds_dwordx4 v210, s[44:45]
	s_add_i32 m0, s26, 0x10000
	s_nop 0
	global_load_lds_dwordx4 v212, s[36:37]
	s_add_i32 m0, s26, 0x16000
	s_cmp_eq_u32 s10, 1
	global_load_lds_dwordx4 v212, s[44:45]
	s_waitcnt vmcnt(0)
	s_cselect_b64 s[44:45], -1, 0
	s_cmp_lg_u32 s10, 1
	s_barrier
	s_cbranch_scc1 .LBB0_683
	s_barrier
.LBB0_683:
	s_add_u32 s46, s42, 0x30000
	s_addc_u32 s47, s43, 0
	s_add_u32 s48, s42, 0x53700000
	s_addc_u32 s49, s43, 0
	s_add_u32 s50, s42, 0x53713800
	s_addc_u32 s51, s43, 0
	s_and_b32 s7, s7, 3
	s_lshl_b32 s27, s10, 6
	s_lshl_b32 s28, s7, 5
	s_cmp_gt_i32 s30, 63
	s_cselect_b64 s[52:53], -1, 0
	s_cmpk_lt_u32 s29, 0x100
	s_cselect_b64 s[54:55], -1, 0
	s_cmp_eq_u32 s7, 0
	v_and_b32_e32 v205, 15, v2
	s_cselect_b64 s[56:57], -1, 0
	s_cmp_ge_i32 s0, s13
	v_bfe_u32 v214, v2, 4, 2
	v_or_b32_e32 v2, s27, v205
	s_cselect_b64 s[58:59], -1, 0
	s_add_i32 s30, s16, s2
	s_mul_i32 s10, s2, s76
	s_sub_i32 s31, s76, s13
	s_sub_i32 s11, s0, s13
	v_mul_lo_u32 v215, v2, s87
	v_or_b32_e32 v2, s28, v205
	s_mul_hi_i32 s7, s2, s76
	s_add_u32 s66, s10, s11
	v_mov_b32_e32 v211, v1
	v_mov_b32_e32 v213, v1
	v_mul_u32_u24_e32 v216, 24, v214
	v_bfe_u32 v218, v205, 3, 1
	v_lshlrev_b32_e32 v218, 4, v218
	v_add_u32_e32 v219, 8, v216
	v_add_u32_e32 v220, 16, v216
	v_xor_b32_e32 v216, v216, v218
	v_xor_b32_e32 v219, v219, v218
	v_xor_b32_e32 v220, v220, v218
	v_mul_u32_u24_e32 v217, 0x60, v2
	s_mov_b32 s29, 0
	s_addc_u32 s67, s7, 0
	s_ashr_i32 s68, s0, 31
	s_mov_b32 s69, 0
	s_branch .LBB0_686

.LBB0_700:
	s_add_i32 s7, s72, 2
	s_cmp_lt_i32 s7, s1
	s_cselect_b64 s[10:11], -1, 0
	s_and_b64 s[74:75], s[10:11], exec
	s_cselect_b32 s73, 0, s1
	s_sub_i32 s7, s7, s73
	s_and_b64 s[74:75], s[10:11], exec
	s_cselect_b32 s74, s38, s60
	s_mul_hi_u32 s77, s7, 0x6000
	s_mulk_i32 s7, 0x6000
	s_cselect_b32 s73, s39, s61
	s_add_u32 s74, s74, s7
	s_addc_u32 s75, s73, s77
	s_and_b64 s[10:11], s[10:11], exec
	s_cselect_b32 s10, s40, s62
	s_cselect_b32 s11, s41, s63
	s_add_u32 s10, s10, s7
	s_addc_u32 s11, s11, s77
	s_cmp_gt_i32 s29, 0
	s_cselect_b32 s7, -1, 2
	s_add_i32 s7, s7, s29
	s_mul_i32 s7, s7, 0xc000
	s_add_i32 s7, s26, s7
	s_add_i32 s73, s7, 0x6000
	v_lshl_add_u64 v[2:3], s[74:75], 0, v[0:1]
	s_mov_b32 m0, s7
	s_andn2_b64 vcc, exec, s[44:45]
	global_load_lds_dwordx4 v[2:3], off
	v_lshl_add_u64 v[2:3], s[10:11], 0, v[0:1]
	s_mov_b32 m0, s73
	s_nop 0
	global_load_lds_dwordx4 v[2:3], off
	v_lshl_add_u64 v[2:3], s[74:75], 0, v[210:211]
	s_add_i32 m0, s7, 0x2000
	s_nop 0
	global_load_lds_dwordx4 v[2:3], off
	v_lshl_add_u64 v[2:3], s[10:11], 0, v[210:211]
	s_add_i32 m0, s7, 0x8000
	s_nop 0
	global_load_lds_dwordx4 v[2:3], off
	v_lshl_add_u64 v[2:3], s[74:75], 0, v[212:213]
	s_add_i32 m0, s7, 0x4000
	s_nop 0
	global_load_lds_dwordx4 v[2:3], off
	v_lshl_add_u64 v[2:3], s[10:11], 0, v[212:213]
	s_add_i32 m0, s7, 0xa000
	s_mul_i32 s7, s29, 0xc000
	global_load_lds_dwordx4 v[2:3], off
	s_add_i32 s7, s7, 0
	v_add3_u32 v221, s7, v217, v216
	v_add3_u32 v222, s7, v217, v219
	v_add3_u32 v6, s7, v217, v220
	v_add3_u32 v223, s7, v215, v216
	v_add3_u32 v224, s7, v215, v219
	v_add3_u32 v18, s7, v215, v220
	ds_read_b64 v[38:39], v221 offset:24576
	ds_read_b64 v[40:41], v222 offset:24576
	ds_read_b64 v[42:43], v6 offset:24576
	ds_read_b64 v[26:27], v221 offset:26112
	ds_read_b64 v[28:29], v222 offset:26112
	ds_read_b64 v[30:31], v6 offset:26112
	ds_read_b64 v[8:9], v221 offset:36864
	ds_read_b64 v[10:11], v222 offset:36864
	ds_read_b64 v[12:13], v6 offset:36864
	ds_read_b64 v[2:3], v221 offset:38400
	ds_read_b64 v[4:5], v222 offset:38400
	ds_read_b64 v[6:7], v6 offset:38400
	ds_read_b64 v[68:69], v223
	ds_read_b64 v[70:71], v224
	ds_read_b64 v[72:73], v18
	ds_read_b64 v[62:63], v223 offset:1536
	ds_read_b64 v[64:65], v224 offset:1536
	ds_read_b64 v[66:67], v18 offset:1536
	ds_read_b64 v[56:57], v223 offset:3072
	ds_read_b64 v[58:59], v224 offset:3072
	ds_read_b64 v[60:61], v18 offset:3072
	ds_read_b64 v[50:51], v223 offset:4608
	ds_read_b64 v[52:53], v224 offset:4608
	ds_read_b64 v[54:55], v18 offset:4608
	ds_read_b64 v[44:45], v223 offset:12288
	ds_read_b64 v[46:47], v224 offset:12288
	ds_read_b64 v[48:49], v18 offset:12288
	ds_read_b64 v[32:33], v223 offset:13824
	ds_read_b64 v[34:35], v224 offset:13824
	ds_read_b64 v[36:37], v18 offset:13824
	ds_read_b64 v[20:21], v223 offset:15360
	ds_read_b64 v[22:23], v224 offset:15360
	ds_read_b64 v[24:25], v18 offset:15360
	ds_read_b64 v[14:15], v223 offset:16896
	ds_read_b64 v[16:17], v224 offset:16896
	ds_read_b64 v[18:19], v18 offset:16896
	s_cbranch_vccnz .LBB0_702
	s_waitcnt vmcnt(6)

.LBB0_764:
	s_andn2_b64 vcc, exec, s[38:39]
	s_cbranch_vccnz .LBB0_838
	s_ashr_i32 s1, s30, 31
	s_lshr_b32 s1, s1, 26
	s_add_i32 s1, s30, s1
	s_ashr_i32 s1, s1, 6
	s_mul_i32 s23, s1, 0x6000
	s_ashr_i32 s26, s59, 31
	s_mul_hi_i32 s17, s1, 0x6000
	s_mul_i32 s26, s23, s26
	s_mul_hi_u32 s27, s23, s59
	s_ashr_i32 s7, s29, 6
	s_add_i32 s26, s27, s26
	s_mul_i32 s27, s17, s59
	s_ashr_i32 s10, s29, 8
	s_lshl_b32 s11, s7, 10
	s_add_i32 s26, s26, s27
	s_mul_i32 s27, s23, s59
	s_add_u32 s38, s3, s27
	s_addc_u32 s39, s5, s26
	s_ashr_i32 s26, s58, 31
	s_mul_i32 s26, s23, s26
	s_mul_hi_u32 s27, s23, s58
	s_add_i32 s26, s27, s26
	s_mul_i32 s27, s17, s58
	s_add_i32 s26, s26, s27
	s_mul_i32 s27, s23, s58
	s_add_u32 s40, s8, s27
	s_addc_u32 s41, s12, s26
	s_add_i32 s26, s11, 0
	v_lshlrev_b32_e32 v0, 4, v2
	v_add_u32_e32 v210, 0x2000, v0
	v_add_u32_e32 v212, 0x4000, v0
	v_mul_u32_u24_e32 v218, 0x2aab, v2
	v_bfe_u32 v218, v218, 19, 1
	v_lshlrev_b32_e32 v218, 4, v218
	v_xor_b32_e32 v0, v0, v218
	v_add_u32_e32 v218, 0x200, v2
	v_mul_u32_u24_e32 v218, 0x2aab, v218
	v_bfe_u32 v218, v218, 19, 1
	v_lshlrev_b32_e32 v218, 4, v218
	v_xor_b32_e32 v210, v210, v218
	v_add_u32_e32 v218, 0x400, v2
	v_mul_u32_u24_e32 v218, 0x2aab, v218
	v_bfe_u32 v218, v218, 19, 1
	v_lshlrev_b32_e32 v218, 4, v218
	v_xor_b32_e32 v212, v212, v218
	s_add_i32 s11, s26, 0x6000
	s_mov_b32 m0, s26
	global_load_lds_dwordx4 v0, s[38:39]
	s_mov_b32 m0, s11
	global_load_lds_dwordx4 v0, s[40:41]
	s_add_i32 m0, s26, 0x2000
	s_nop 0
	global_load_lds_dwordx4 v210, s[38:39]
	s_add_i32 m0, s26, 0x8000
	s_nop 0
	global_load_lds_dwordx4 v210, s[40:41]
	s_add_i32 m0, s26, 0x4000
	s_nop 0
	global_load_lds_dwordx4 v212, s[38:39]
	s_add_i32 m0, s26, 0xa000
	s_add_u32 s36, s38, 0x6000
	global_load_lds_dwordx4 v212, s[40:41]
	s_addc_u32 s37, s39, 0
	s_add_i32 m0, s26, 0xc000
	s_add_u32 s44, s40, 0x6000
	s_addc_u32 s45, s41, 0
	s_add_i32 s11, s26, 0x12000
	global_load_lds_dwordx4 v0, s[36:37]
	s_mov_b32 m0, s11
	s_nop 0
	global_load_lds_dwordx4 v0, s[44:45]
	s_add_i32 m0, s26, 0xe000
	s_nop 0
	global_load_lds_dwordx4 v210, s[36:37]
	s_add_i32 m0, s26, 0x14000
	s_nop 0
	global_load_lds_dwordx4 v210, s[44:45]
	s_add_i32 m0, s26, 0x10000
	s_nop 0
	global_load_lds_dwordx4 v212, s[36:37]
	s_add_i32 m0, s26, 0x16000
	s_cmp_eq_u32 s10, 1
	global_load_lds_dwordx4 v212, s[44:45]
	s_waitcnt vmcnt(0)
	s_cselect_b64 s[44:45], -1, 0
	s_cmp_lg_u32 s10, 1
	s_barrier
	s_cbranch_scc1 .LBB0_767
	s_barrier
.LBB0_767:
	s_add_u32 s42, s42, 0x15e000
	s_addc_u32 s43, s43, 0
	s_and_b32 s7, s7, 3
	s_lshl_b32 s27, s10, 6
	s_lshl_b32 s28, s7, 5
	s_cmp_gt_i32 s30, 63
	s_cselect_b64 s[46:47], -1, 0
	s_cmpk_lt_u32 s29, 0x100
	s_cselect_b64 s[48:49], -1, 0
	s_cmp_eq_u32 s7, 0
	v_and_b32_e32 v205, 15, v2
	s_cselect_b64 s[50:51], -1, 0
	s_cmp_ge_i32 s0, s13
	v_bfe_u32 v214, v2, 4, 2
	v_or_b32_e32 v2, s27, v205
	s_cselect_b64 s[52:53], -1, 0
	s_add_i32 s16, s16, s2
	s_mul_i32 s10, s2, s76
	s_sub_i32 s30, s76, s13
	s_sub_i32 s11, s0, s13
	v_mul_lo_u32 v215, v2, s87
	v_or_b32_e32 v2, s28, v205
	s_mul_hi_i32 s7, s2, s76
	s_add_u32 s13, s10, s11
	v_mov_b32_e32 v211, v1
	v_mov_b32_e32 v213, v1
	v_mul_u32_u24_e32 v216, 24, v214
	v_bfe_u32 v218, v205, 3, 1
	v_lshlrev_b32_e32 v218, 4, v218
	v_add_u32_e32 v219, 8, v216
	v_add_u32_e32 v220, 16, v216
	v_xor_b32_e32 v216, v216, v218
	v_xor_b32_e32 v219, v219, v218
	v_xor_b32_e32 v220, v220, v218
	v_mul_u32_u24_e32 v217, 0x60, v2
	s_mov_b32 s29, 0
	s_addc_u32 s31, s7, 0
	s_ashr_i32 s60, s0, 31
	s_mov_b32 s61, 0
	s_branch .LBB0_770

.LBB0_784:
	s_add_i32 s7, s64, 2
	s_cmp_lt_i32 s7, s1
	s_cselect_b64 s[10:11], -1, 0
	s_and_b64 s[66:67], s[10:11], exec
	s_cselect_b32 s65, 0, s1
	s_sub_i32 s7, s7, s65
	s_and_b64 s[66:67], s[10:11], exec
	s_cselect_b32 s66, s38, s54
	s_mul_hi_u32 s68, s7, 0x6000
	s_mulk_i32 s7, 0x6000
	s_cselect_b32 s65, s39, s55
	s_add_u32 s66, s66, s7
	s_addc_u32 s67, s65, s68
	s_and_b64 s[10:11], s[10:11], exec
	s_cselect_b32 s10, s40, s56
	s_cselect_b32 s11, s41, s57
	s_add_u32 s10, s10, s7
	s_addc_u32 s11, s11, s68
	s_cmp_gt_i32 s29, 0
	s_cselect_b32 s7, -1, 2
	s_add_i32 s7, s7, s29
	s_mul_i32 s7, s7, 0xc000
	s_add_i32 s7, s26, s7
	s_add_i32 s65, s7, 0x6000
	v_lshl_add_u64 v[2:3], s[66:67], 0, v[0:1]
	s_mov_b32 m0, s7
	s_andn2_b64 vcc, exec, s[44:45]
	global_load_lds_dwordx4 v[2:3], off
	v_lshl_add_u64 v[2:3], s[10:11], 0, v[0:1]
	s_mov_b32 m0, s65
	s_nop 0
	global_load_lds_dwordx4 v[2:3], off
	v_lshl_add_u64 v[2:3], s[66:67], 0, v[210:211]
	s_add_i32 m0, s7, 0x2000
	s_nop 0
	global_load_lds_dwordx4 v[2:3], off
	v_lshl_add_u64 v[2:3], s[10:11], 0, v[210:211]
	s_add_i32 m0, s7, 0x8000
	s_nop 0
	global_load_lds_dwordx4 v[2:3], off
	v_lshl_add_u64 v[2:3], s[66:67], 0, v[212:213]
	s_add_i32 m0, s7, 0x4000
	s_nop 0
	global_load_lds_dwordx4 v[2:3], off
	v_lshl_add_u64 v[2:3], s[10:11], 0, v[212:213]
	s_add_i32 m0, s7, 0xa000
	s_mul_i32 s7, s29, 0xc000
	global_load_lds_dwordx4 v[2:3], off
	s_add_i32 s7, s7, 0
	v_add3_u32 v221, s7, v217, v216
	v_add3_u32 v222, s7, v217, v219
	v_add3_u32 v6, s7, v217, v220
	v_add3_u32 v223, s7, v215, v216
	v_add3_u32 v224, s7, v215, v219
	v_add3_u32 v18, s7, v215, v220
	ds_read_b64 v[38:39], v221 offset:24576
	ds_read_b64 v[40:41], v222 offset:24576
	ds_read_b64 v[42:43], v6 offset:24576
	ds_read_b64 v[26:27], v221 offset:26112
	ds_read_b64 v[28:29], v222 offset:26112
	ds_read_b64 v[30:31], v6 offset:26112
	ds_read_b64 v[8:9], v221 offset:36864
	ds_read_b64 v[10:11], v222 offset:36864
	ds_read_b64 v[12:13], v6 offset:36864
	ds_read_b64 v[2:3], v221 offset:38400
	ds_read_b64 v[4:5], v222 offset:38400
	ds_read_b64 v[6:7], v6 offset:38400
	ds_read_b64 v[68:69], v223
	ds_read_b64 v[70:71], v224
	ds_read_b64 v[72:73], v18
	ds_read_b64 v[62:63], v223 offset:1536
	ds_read_b64 v[64:65], v224 offset:1536
	ds_read_b64 v[66:67], v18 offset:1536
	ds_read_b64 v[56:57], v223 offset:3072
	ds_read_b64 v[58:59], v224 offset:3072
	ds_read_b64 v[60:61], v18 offset:3072
	ds_read_b64 v[50:51], v223 offset:4608
	ds_read_b64 v[52:53], v224 offset:4608
	ds_read_b64 v[54:55], v18 offset:4608
	ds_read_b64 v[44:45], v223 offset:12288
	ds_read_b64 v[46:47], v224 offset:12288
	ds_read_b64 v[48:49], v18 offset:12288
	ds_read_b64 v[32:33], v223 offset:13824
	ds_read_b64 v[34:35], v224 offset:13824
	ds_read_b64 v[36:37], v18 offset:13824
	ds_read_b64 v[20:21], v223 offset:15360
	ds_read_b64 v[22:23], v224 offset:15360
	ds_read_b64 v[24:25], v18 offset:15360
	ds_read_b64 v[14:15], v223 offset:16896
	ds_read_b64 v[16:17], v224 offset:16896
	ds_read_b64 v[18:19], v18 offset:16896
	s_cbranch_vccnz .LBB0_786
	s_waitcnt vmcnt(6)
